# baseline (speedup 1.0000x reference)
_Z16rec_chunk_kernelPKDF16_PKfS2_S2_PfS3_:
	s_load_dwordx4 s[12:15], s[0:1], 0x0
	s_cmpk_lt_u32 s2, 0xc0
	s_mov_b64 s[4:5], -1
	s_cbranch_scc0 .LBB2_4
	s_load_dwordx8 s[4:11], s[0:1], 0x10
	s_bfe_u32 s1, s2, 0x80003
	s_mulk_i32 s1, 0xab
	s_lshr_b32 s1, s1, 10
	s_lshr_b32 s0, s2, 3
	s_mul_i32 s1, s1, 6
	s_sub_i32 s0, s0, s1
	s_and_b32 s22, s0, 0xff
	s_lshl_b32 s0, s2, 2
	s_and_b32 s23, s0, 28
	s_and_b32 s0, s2, 0xff
	s_mulk_i32 s0, 0xab
	s_lshr_b32 s33, s0, 13
	s_add_i32 s23, s23, s33
	s_mov_b32 s19, 0x20000
	s_mov_b32 s18, 0xa80000
	s_waitcnt lgkmcnt(0)
	s_and_b32 s17, s13, 0xffff
	s_mul_i32 s3, s23, 0x54000
	s_mov_b32 s28, s12
	s_mov_b32 s29, s17
	s_mov_b32 s30, s18
	s_mov_b32 s31, s19
	v_lshlrev_b32_e32 v1, 4, v0
	s_or_b32 s1, s3, 0x1800
	s_and_b32 s21, s9, 0xffff
	buffer_load_dwordx4 v[162:165], v1, s[28:31], s3 offen
	buffer_load_dwordx4 v[158:161], v1, s[28:31], s1 offen
	s_or_b32 s1, s3, 0x3000
	s_add_i32 s9, s3, 0x4800
	buffer_load_dwordx4 v[154:157], v1, s[28:31], s1 offen
	buffer_load_dwordx4 v[178:181], v1, s[28:31], s9 offen
	s_or_b32 s1, s3, 0x400
	s_or_b32 s9, s3, 0x1c00
	buffer_load_dwordx4 v[186:189], v1, s[28:31], s1 offen
	buffer_load_dwordx4 v[190:193], v1, s[28:31], s9 offen
	s_or_b32 s1, s3, 0x3400
	s_add_i32 s9, s3, 0x4c00
	buffer_load_dwordx4 v[194:197], v1, s[28:31], s1 offen
	buffer_load_dwordx4 v[182:185], v1, s[28:31], s9 offen
	s_or_b32 s1, s3, 0x800
	s_or_b32 s9, s3, 0x2000
	buffer_load_dwordx4 v[150:153], v1, s[28:31], s1 offen
	buffer_load_dwordx4 v[138:141], v1, s[28:31], s9 offen
	s_or_b32 s1, s3, 0x3800
	s_add_i32 s9, s3, 0x5000
	buffer_load_dwordx4 v[146:149], v1, s[28:31], s1 offen
	buffer_load_dwordx4 v[134:137], v1, s[28:31], s9 offen
	s_or_b32 s1, s3, 0xc00
	s_or_b32 s9, s3, 0x2400
	buffer_load_dwordx4 v[142:145], v1, s[28:31], s1 offen
	buffer_load_dwordx4 v[170:173], v1, s[28:31], s9 offen
	s_or_b32 s1, s3, 0x3c00
	s_add_i32 s9, s3, 0x5400
	s_mul_i32 s0, s23, 48
	buffer_load_dwordx4 v[174:177], v1, s[28:31], s1 offen
	buffer_load_dwordx4 v[166:169], v1, s[28:31], s9 offen
	s_or_b32 s1, s3, 0x1000
	s_or_b32 s9, s3, 0x2800
	s_or_b32 s0, s0, s22
	buffer_load_dwordx4 v[122:125], v1, s[28:31], s1 offen
	buffer_load_dwordx4 v[130:133], v1, s[28:31], s9 offen
	s_add_i32 s1, s3, 0x4000
	s_add_i32 s9, s3, 0x5800
	s_mov_b32 s26, 0xc00000
	buffer_load_dwordx4 v[126:129], v1, s[28:31], s1 offen
	buffer_load_dwordx4 v[114:117], v1, s[28:31], s9 offen
	s_or_b32 s1, s3, 0x1400
	s_and_b32 s25, s15, 0xffff
	s_lshl_b32 s9, s0, 13
	buffer_load_dwordx4 v[118:121], v1, s[28:31], s1 offen
	s_mov_b32 s28, s14
	s_mov_b32 s29, s25
	s_mov_b32 s30, s26
	s_or_b32 s0, s9, 0x400
	buffer_load_dwordx4 v[50:53], v1, s[28:31], s9 offen
	buffer_load_dwordx4 v[54:57], v1, s[28:31], s0 offen
	s_or_b32 s0, s9, 0x800
	s_or_b32 s35, s9, 0xc00
	buffer_load_dwordx4 v[58:61], v1, s[28:31], s0 offen
	buffer_load_dwordx4 v[62:65], v1, s[28:31], s35 offen
	s_or_b32 s0, s9, 0x1000
	s_lshr_b32 s1, s23, 3
	s_or_b32 s35, s9, 0x1400
	buffer_load_dwordx4 v[66:69], v1, s[28:31], s0 offen
	buffer_load_dwordx4 v[70:73], v1, s[28:31], s35 offen
	s_or_b32 s0, s9, 0x1800
	s_or_b32 s35, s9, 0x1c00
	buffer_load_dwordx4 v[74:77], v1, s[28:31], s0 offen
	buffer_load_dwordx4 v[78:81], v1, s[28:31], s35 offen
	s_mul_i32 s0, s23, 0x4800
	s_mulk_i32 s1, 0x3000
	s_add_i32 s1, s1, s0
	v_lshrrev_b32_e32 v2, 3, v0
	s_lshl_b32 s0, s22, 7
	s_lshl_b32 s1, s1, 2
	v_and_b32_e32 v2, 4, v2
	s_or_b32 s28, s1, s0
	v_mul_u32_u24_e32 v2, 0xc0, v2
	s_add_u32 s0, s6, s28
	v_and_or_b32 v2, v0, 31, v2
	s_addc_u32 s1, s7, 0
	v_lshlrev_b32_e32 v226, 2, v2
	v_mov_b32_e32 v227, 0
	s_movk_i32 s27, 0x1000
	v_lshl_add_u64 v[30:31], s[0:1], 0, v[226:227]
	v_add_co_u32_e32 v2, vcc, s27, v30
	s_movk_i32 s20, 0x2000
	s_nop 0
	v_addc_co_u32_e32 v3, vcc, 0, v31, vcc
	v_add_co_u32_e32 v4, vcc, s20, v30
	s_movk_i32 s16, 0x3000
	s_nop 0
	v_addc_co_u32_e32 v5, vcc, 0, v31, vcc
	v_add_co_u32_e32 v6, vcc, s16, v30
	s_movk_i32 s34, 0x4000
	s_nop 0
	v_addc_co_u32_e32 v7, vcc, 0, v31, vcc
	global_load_dword v38, v[2:3], off offset:2048
	global_load_dword v39, v[2:3], off offset:2816
	global_load_dword v40, v[2:3], off offset:3584
	global_load_dword v41, v[4:5], off offset:256
	global_load_dword v42, v[6:7], off
	global_load_dword v43, v[6:7], off offset:768
	global_load_dword v44, v[6:7], off offset:1536
	global_load_dword v45, v[6:7], off offset:2304
	v_add_co_u32_e32 v2, vcc, s34, v30
	s_movk_i32 s24, 0x5000
	s_nop 0
	v_addc_co_u32_e32 v3, vcc, 0, v31, vcc
	v_add_co_u32_e32 v4, vcc, s24, v30
	s_movk_i32 s6, 0x6000
	s_nop 0
	v_addc_co_u32_e32 v5, vcc, 0, v31, vcc
	v_add_co_u32_e32 v6, vcc, s6, v30
	s_movk_i32 s6, 0x7000
	s_nop 0
	v_addc_co_u32_e32 v7, vcc, 0, v31, vcc
	v_add_co_u32_e32 v8, vcc, s6, v30
	s_mov_b32 s6, 0x8000
	s_nop 0
	v_addc_co_u32_e32 v9, vcc, 0, v31, vcc
	v_add_co_u32_e32 v10, vcc, s6, v30
	s_mov_b32 s6, 0x9000
	s_nop 0
	v_addc_co_u32_e32 v11, vcc, 0, v31, vcc
	v_add_co_u32_e32 v14, vcc, s6, v30
	s_mov_b32 s6, 0xa000
	s_nop 0
	v_addc_co_u32_e32 v15, vcc, 0, v31, vcc
	v_add_co_u32_e32 v16, vcc, s6, v30
	s_mov_b32 s6, 0xb000
	s_nop 0
	v_addc_co_u32_e32 v17, vcc, 0, v31, vcc
	v_add_co_u32_e32 v18, vcc, s6, v30
	s_mov_b32 s6, 0xc000
	s_nop 0
	v_addc_co_u32_e32 v19, vcc, 0, v31, vcc
	v_add_co_u32_e32 v22, vcc, s6, v30
	s_mov_b32 s6, 0xd000
	s_nop 0
	v_addc_co_u32_e32 v23, vcc, 0, v31, vcc
	v_add_co_u32_e32 v24, vcc, s6, v30
	s_mov_b32 s6, 0xe000
	s_nop 0
	v_addc_co_u32_e32 v25, vcc, 0, v31, vcc
	v_add_co_u32_e32 v26, vcc, s6, v30
	s_mov_b32 s6, 0xf000
	s_nop 0
	v_addc_co_u32_e32 v27, vcc, 0, v31, vcc
	v_add_co_u32_e32 v32, vcc, s6, v30
	s_mov_b32 s6, 0x10000
	s_nop 0
	v_addc_co_u32_e32 v33, vcc, 0, v31, vcc
	global_load_dword v46, v[2:3], off offset:2048
	global_load_dword v47, v[2:3], off offset:2816
	global_load_dword v48, v[2:3], off offset:3584
	global_load_dword v49, v[4:5], off offset:256
	s_nop 0
	global_load_dword v2, v[6:7], off
	global_load_dword v3, v[6:7], off offset:768
	global_load_dword v4, v[6:7], off offset:1536
	global_load_dword v5, v[6:7], off offset:2304
	s_nop 0
	global_load_dword v6, v[8:9], off offset:2048
	global_load_dword v7, v[8:9], off offset:2816
	s_nop 0
	global_load_dword v8, v[8:9], off offset:3584
	s_nop 0
	global_load_dword v9, v[10:11], off offset:256
	s_nop 0
	global_load_dword v10, v[14:15], off
	global_load_dword v11, v[14:15], off offset:768
	global_load_dword v12, v[14:15], off offset:1536
	global_load_dword v13, v[14:15], off offset:2304
	s_nop 0
	global_load_dword v14, v[16:17], off offset:2048
	global_load_dword v15, v[16:17], off offset:2816
	s_nop 0
	global_load_dword v16, v[16:17], off offset:3584
	s_nop 0
	global_load_dword v17, v[18:19], off offset:256
	s_nop 0
	global_load_dword v18, v[22:23], off
	global_load_dword v19, v[22:23], off offset:768
	global_load_dword v20, v[22:23], off offset:1536
	global_load_dword v21, v[22:23], off offset:2304
	s_nop 0
	global_load_dword v22, v[24:25], off offset:2048
	global_load_dword v23, v[24:25], off offset:2816
	s_nop 0
	global_load_dword v24, v[24:25], off offset:3584
	s_nop 0
	global_load_dword v25, v[26:27], off offset:256
	s_nop 0
	global_load_dword v26, v[32:33], off
	global_load_dword v27, v[32:33], off offset:768
	global_load_dword v28, v[32:33], off offset:1536
	global_load_dword v29, v[32:33], off offset:2304
	v_add_co_u32_e32 v32, vcc, s6, v30
	s_mov_b32 s6, 0x11000
	s_nop 0
	v_addc_co_u32_e32 v33, vcc, 0, v31, vcc
	v_add_co_u32_e32 v82, vcc, s6, v30
	s_mov_b32 s16, s12
	s_nop 0
	v_addc_co_u32_e32 v83, vcc, 0, v31, vcc
	global_load_dword v34, v226, s[0:1]
	global_load_dword v35, v226, s[0:1] offset:768
	global_load_dword v36, v226, s[0:1] offset:1536
	global_load_dword v37, v226, s[0:1] offset:2304
	global_load_dword v30, v[32:33], off offset:2048
	global_load_dword v31, v[32:33], off offset:2816
	s_nop 0
	global_load_dword v32, v[32:33], off offset:3584
	s_nop 0
	global_load_dword v33, v[82:83], off offset:256
	s_mov_b32 s20, s8
	s_mov_b32 s27, s19
	s_mov_b32 s24, s14
	s_mov_b32 s6, 0
	s_and_b32 s0, s2, 7
	s_mulk_i32 s0, 0xc0
	s_mul_i32 s33, s33, 48
	s_add_i32 s0, s0, s33
	s_or_b32 s0, s0, s22
	s_lshl_b32 s0, s0, 13
	s_or_b32 s7, s0, 0x1c00
	s_lshl_b32 s0, s23, 5
	s_add_u32 s0, s4, s0
	s_addc_u32 s1, s5, 0
	s_load_dwordx8 s[40:47], s[0:1], 0x0
	s_mov_b32 s4, 1
.LBB2_2:
	s_cmp_lg_u32 s6, 0x49800
	s_cselect_b32 s22, s4, 7
	s_add_i32 s8, s3, s6
	s_add_i32 s5, s8, 0x2c00
	s_add_i32 s23, s8, 0x4400
	buffer_load_dwordx4 v[214:217], v1, s[16:19], s5 offen
	buffer_load_dwordx4 v[210:213], v1, s[16:19], s23 offen
	s_add_i32 s5, s8, 0x5c00
	s_add_i32 s23, s8, 0x7800
	buffer_load_dwordx4 v[206:209], v1, s[16:19], s5 offen
	buffer_load_dwordx4 v[198:201], v1, s[16:19], s23 offen
	s_waitcnt vmcnt(48)
	v_cvt_pk_f16_f32 v85, v40, v41
	v_cvt_pk_f16_f32 v84, v38, v39
	s_waitcnt vmcnt(8)
	v_cvt_pk_f16_f32 v83, v36, v37
	v_cvt_pk_f16_f32 v82, v34, v35
	s_mul_i32 s5, s22, 0xa800
	s_add_i32 s5, s5, s3
	v_mfma_f32_32x32x16_f16 v[50:65], v[162:165], v[82:85], v[50:65]
	v_cvt_pk_f16_f32 v165, v48, v49
	v_cvt_pk_f16_f32 v164, v46, v47
	v_cvt_pk_f16_f32 v163, v44, v45
	v_cvt_pk_f16_f32 v162, v42, v43
	s_mul_i32 s22, s22, 0xc000
	s_waitcnt lgkmcnt(0)
	s_mov_b32 s23, s40
	v_mul_f32 v34, s23, v34
	v_mfma_f32_32x32x16_f16 v[66:81], v[158:161], v[82:85], v[66:81]
	v_mul_f32 v35, s23, v35
	v_mul_f32 v36, s23, v36
	v_mul_f32 v37, s23, v37
	v_mul_f32 v38, s23, v38
	v_mul_f32 v39, s23, v39
	v_mul_f32 v40, s23, v40
	v_mul_f32 v41, s23, v41
	v_mul_f32 v42, s23, v42
	v_mfma_f32_32x32x16_f16 v[98:113], v[154:157], v[82:85], 0
	v_mul_f32 v43, s23, v43
	v_mul_f32 v44, s23, v44
	v_mul_f32 v45, s23, v45
	v_mul_f32 v46, s23, v46
	v_mul_f32 v47, s23, v47
	v_mul_f32 v48, s23, v48
	v_mul_f32 v49, s23, v49
	v_mfma_f32_32x32x16_f16 v[82:97], v[178:181], v[82:85], 0
	s_add_i32 s29, s8, 0x8800
	v_mfma_f32_32x32x16_f16 v[50:65], v[186:189], v[162:165], v[50:65]
	s_add_i32 s30, s8, 0x9800
	v_mfma_f32_32x32x16_f16 v[66:81], v[190:193], v[162:165], v[66:81]
	buffer_load_dwordx4 v[190:193], v1, s[16:19], s29 offen
	buffer_load_dwordx4 v[186:189], v1, s[16:19], s30 offen
	s_add_i32 s29, s8, 0x6000
	s_add_i32 s30, s8, 0x6800
	buffer_load_dwordx4 v[178:181], v1, s[16:19], s29 offen
	buffer_load_dwordx4 v[202:205], v1, s[16:19], s30 offen
	v_mfma_f32_32x32x16_f16 v[98:113], v[194:197], v[162:165], v[98:113]
	v_mfma_f32_32x32x16_f16 v[82:97], v[182:185], v[162:165], v[82:97]
	s_add_i32 s29, s8, 0x7c00
	v_cvt_pk_f16_f32 v157, v8, v9
	v_cvt_pk_f16_f32 v156, v6, v7
	v_cvt_pk_f16_f32 v155, v4, v5
	v_cvt_pk_f16_f32 v154, v2, v3
	s_add_i32 s30, s8, 0x8c00
	buffer_load_dwordx4 v[228:231], v1, s[16:19], s29 offen
	buffer_load_dwordx4 v[222:225], v1, s[16:19], s30 offen
	s_add_i32 s29, s8, 0x9c00
	v_mfma_f32_32x32x16_f16 v[50:65], v[150:153], v[154:157], v[50:65]
	s_add_i32 s30, s8, 0x6400
	buffer_load_dwordx4 v[232:235], v1, s[16:19], s29 offen
	buffer_load_dwordx4 v[150:153], v1, s[16:19], s30 offen
	v_cvt_pk_f16_f32 v161, v16, v17
	v_cvt_pk_f16_f32 v160, v14, v15
	v_cvt_pk_f16_f32 v159, v12, v13
	v_cvt_pk_f16_f32 v158, v10, v11
	v_mul_f32 v2, s23, v2
	v_mfma_f32_32x32x16_f16 v[66:81], v[138:141], v[154:157], v[66:81]
	v_mul_f32 v3, s23, v3
	v_mul_f32 v4, s23, v4
	v_mul_f32 v5, s23, v5
	v_mul_f32 v6, s23, v6
	v_mul_f32 v7, s23, v7
	v_mul_f32 v8, s23, v8
	v_mul_f32 v9, s23, v9
	v_mul_f32 v10, s23, v10
	v_mfma_f32_32x32x16_f16 v[98:113], v[146:149], v[154:157], v[98:113]
	v_mul_f32 v11, s23, v11
	v_mul_f32 v12, s23, v12
	v_mul_f32 v13, s23, v13
	v_mul_f32 v14, s23, v14
	v_mul_f32 v15, s23, v15
	v_mul_f32 v16, s23, v16
	v_mul_f32 v17, s23, v17
	v_mfma_f32_32x32x16_f16 v[82:97], v[134:137], v[154:157], v[82:97]
	s_add_i32 s29, s8, 0x6c00
	v_mfma_f32_32x32x16_f16 v[98:113], v[174:177], v[158:161], v[98:113]
	s_add_i32 s30, s8, 0x8000
	buffer_load_dwordx4 v[236:239], v1, s[16:19], s29 offen
	buffer_load_dwordx4 v[174:177], v1, s[16:19], s30 offen
	s_add_i32 s29, s8, 0x9000
	s_add_i32 s30, s8, 0xa000
	v_mfma_f32_32x32x16_f16 v[66:81], v[170:173], v[158:161], v[66:81]
	buffer_load_dwordx4 v[218:221], v1, s[16:19], s29 offen
	buffer_load_dwordx4 v[170:173], v1, s[16:19], s30 offen
	v_mfma_f32_32x32x16_f16 v[50:65], v[142:145], v[158:161], v[50:65]
	v_mfma_f32_32x32x16_f16 v[82:97], v[166:169], v[158:161], v[82:97]
	s_add_i32 s29, s8, 0x7000
	s_add_i32 s30, s8, 0x8400
	buffer_load_dwordx4 v[240:243], v1, s[16:19], s29 offen
	buffer_load_dwordx4 v[244:247], v1, s[16:19], s30 offen
	s_add_i32 s29, s8, 0x9400
	s_add_i32 s30, s8, 0xa400
	buffer_load_dwordx4 v[248:251], v1, s[16:19], s29 offen
	buffer_load_dwordx4 v[252:255], v1, s[16:19], s30 offen
	v_cvt_pk_f16_f32 v137, v24, v25
	v_cvt_pk_f16_f32 v136, v22, v23
	v_cvt_pk_f16_f32 v135, v20, v21
	v_cvt_pk_f16_f32 v134, v18, v19
	v_mul_f32 v18, s23, v18
	v_mul_f32 v19, s23, v19
	v_mul_f32 v20, s23, v20
	v_mul_f32 v21, s23, v21
	v_mul_f32 v22, s23, v22
	s_nop 1
	v_mfma_f32_32x32x16_f16 v[50:65], v[122:125], v[134:137], v[50:65]
	s_waitcnt vmcnt(20)
	v_cvt_pk_f16_f32 v125, v32, v33
	v_cvt_pk_f16_f32 v124, v30, v31
	v_cvt_pk_f16_f32 v123, v28, v29
	v_cvt_pk_f16_f32 v122, v26, v27
	v_mul_f32 v23, s23, v23
	v_mul_f32 v24, s23, v24
	v_mul_f32 v25, s23, v25
	v_mfma_f32_32x32x16_f16 v[66:81], v[130:133], v[134:137], v[66:81]
	v_mul_f32 v26, s23, v26
	v_mul_f32 v27, s23, v27
	v_mul_f32 v28, s23, v28
	v_mul_f32 v29, s23, v29
	v_mul_f32 v30, s23, v30
	v_mul_f32 v31, s23, v31
	v_mul_f32 v32, s23, v32
	v_mfma_f32_32x32x16_f16 v[98:113], v[126:129], v[134:137], v[98:113]
	v_mul_f32 v33, s23, v33
	v_mfma_f32_32x32x16_f16 v[82:97], v[114:117], v[134:137], v[82:97]
	s_addk_i32 s8, 0x7400
	s_waitcnt vmcnt(18)
	v_mfma_f32_32x32x16_f16 v[98:113], v[210:213], v[122:125], v[98:113]
	buffer_load_dwordx4 v[210:213], v1, s[16:19], s8 offen
	buffer_load_dwordx4 v[162:165], v1, s[16:19], s5 offen
	s_add_i32 s8, s5, 0x1800
	s_add_i32 s23, s5, 0x3000
	buffer_load_dwordx4 v[158:161], v1, s[16:19], s8 offen
	buffer_load_dwordx4 v[154:157], v1, s[16:19], s23 offen
	v_mfma_f32_32x32x16_f16 v[50:65], v[118:121], v[122:125], v[50:65]
	v_mfma_f32_32x32x16_f16 v[66:81], v[214:217], v[122:125], v[66:81]
	s_waitcnt vmcnt(21)
	v_mfma_f32_32x32x16_f16 v[82:97], v[206:209], v[122:125], v[82:97]
	s_nop 8
	v_cvt_pk_f16_f32 v117, v56, v57
	v_cvt_pk_f16_f32 v116, v54, v55
	v_cvt_pk_f16_f32 v115, v52, v53
	v_cvt_pk_f16_f32 v114, v50, v51
	v_cvt_pk_f16_f32 v121, v64, v65
	v_cvt_pk_f16_f32 v120, v62, v63
	v_cvt_pk_f16_f32 v119, v60, v61
	v_cvt_pk_f16_f32 v118, v58, v59
	s_add_i32 s8, s22, s9
	s_or_b32 s22, s8, 0x400
	buffer_load_dwordx4 v[50:53], v1, s[24:27], s8 offen
	buffer_load_dwordx4 v[54:57], v1, s[24:27], s22 offen
	s_or_b32 s22, s8, 0x800
	s_or_b32 s23, s8, 0xc00
	buffer_load_dwordx4 v[58:61], v1, s[24:27], s22 offen
	buffer_load_dwordx4 v[62:65], v1, s[24:27], s23 offen
	s_add_i32 s22, s5, 0x4800
	s_waitcnt vmcnt(22)
	v_mfma_f32_32x32x16_f16 v[18:33], v[186:189], v[114:117], v[18:33]
	s_or_b32 s23, s5, 0x400
	s_waitcnt vmcnt(21)
	v_mfma_f32_32x32x16_f16 v[98:113], v[178:181], v[114:117], v[98:113]
	buffer_load_dwordx4 v[178:181], v1, s[16:19], s22 offen
	buffer_load_dwordx4 v[186:189], v1, s[16:19], s23 offen
	s_add_i32 s22, s5, 0x1c00
	s_add_i32 s23, s5, 0x3400
	v_mfma_f32_32x32x16_f16 v[2:17], v[190:193], v[114:117], v[2:17]
	buffer_load_dwordx4 v[190:193], v1, s[16:19], s22 offen
	buffer_load_dwordx4 v[194:197], v1, s[16:19], s23 offen
	s_add_i32 s22, s5, 0x4c00
	buffer_load_dwordx4 v[182:185], v1, s[16:19], s22 offen
	v_mfma_f32_32x32x16_f16 v[34:49], v[198:201], v[114:117], v[34:49]
	s_waitcnt vmcnt(25)
	v_mfma_f32_32x32x16_f16 v[82:97], v[202:205], v[114:117], v[82:97]
	s_add_i32 s22, s5, 0x800
	s_add_i32 s23, s5, 0x2000
	s_waitcnt vmcnt(21)
	v_mfma_f32_32x32x16_f16 v[98:113], v[150:153], v[118:121], v[98:113]
	buffer_load_dwordx4 v[150:153], v1, s[16:19], s22 offen
	buffer_load_dwordx4 v[138:141], v1, s[16:19], s23 offen
	s_add_i32 s22, s5, 0x3800
	s_add_i32 s23, s5, 0x5000
	buffer_load_dwordx4 v[146:149], v1, s[16:19], s22 offen
	buffer_load_dwordx4 v[134:137], v1, s[16:19], s23 offen
	s_add_i32 s22, s5, 0xc00
	buffer_load_dwordx4 v[142:145], v1, s[16:19], s22 offen
	v_mfma_f32_32x32x16_f16 v[34:49], v[228:231], v[118:121], v[34:49]
	v_mfma_f32_32x32x16_f16 v[2:17], v[222:225], v[118:121], v[2:17]
	v_mfma_f32_32x32x16_f16 v[18:33], v[232:235], v[118:121], v[18:33]
	s_waitcnt vmcnt(25)
	v_mfma_f32_32x32x16_f16 v[82:97], v[236:239], v[118:121], v[82:97]
	v_cvt_pk_f16_f32 v117, v72, v73
	v_cvt_pk_f16_f32 v116, v70, v71
	v_cvt_pk_f16_f32 v115, v68, v69
	v_cvt_pk_f16_f32 v114, v66, v67
	v_cvt_pk_f16_f32 v201, v80, v81
	v_cvt_pk_f16_f32 v200, v78, v79
	v_cvt_pk_f16_f32 v199, v76, v77
	v_cvt_pk_f16_f32 v198, v74, v75
	s_or_b32 s22, s8, 0x1000
	s_or_b32 s23, s8, 0x1400
	buffer_load_dwordx4 v[66:69], v1, s[24:27], s22 offen
	buffer_load_dwordx4 v[70:73], v1, s[24:27], s23 offen
	s_or_b32 s22, s8, 0x1800
	s_or_b32 s8, s8, 0x1c00
	buffer_load_dwordx4 v[74:77], v1, s[24:27], s22 offen
	buffer_load_dwordx4 v[78:81], v1, s[24:27], s8 offen
	s_add_i32 s8, s5, 0x2400
	s_waitcnt vmcnt(28)
	v_mfma_f32_32x32x16_f16 v[34:49], v[174:177], v[114:117], v[34:49]
	s_add_i32 s22, s5, 0x3c00
	s_waitcnt vmcnt(26)
	v_mfma_f32_32x32x16_f16 v[18:33], v[170:173], v[114:117], v[18:33]
	buffer_load_dwordx4 v[170:173], v1, s[16:19], s8 offen
	buffer_load_dwordx4 v[174:177], v1, s[16:19], s22 offen
	s_add_i32 s8, s5, 0x5400
	s_add_i32 s22, s5, 0x1000
	buffer_load_dwordx4 v[166:169], v1, s[16:19], s8 offen
	buffer_load_dwordx4 v[122:125], v1, s[16:19], s22 offen
	v_mfma_f32_32x32x16_f16 v[2:17], v[218:221], v[114:117], v[2:17]
	s_waitcnt vmcnt(29)
	v_mfma_f32_32x32x16_f16 v[82:97], v[240:243], v[114:117], v[82:97]
	s_add_i32 s8, s5, 0x2800
	s_add_i32 s22, s5, 0x4000
	buffer_load_dwordx4 v[130:133], v1, s[16:19], s8 offen
	buffer_load_dwordx4 v[126:129], v1, s[16:19], s22 offen
	s_add_i32 s8, s5, 0x5800
	s_addk_i32 s5, 0x1400
	buffer_load_dwordx4 v[114:117], v1, s[16:19], s8 offen
	buffer_load_dwordx4 v[118:121], v1, s[16:19], s5 offen
	s_waitcnt vmcnt(32)
	v_mfma_f32_32x32x16_f16 v[34:49], v[244:247], v[198:201], v[34:49]
	s_waitcnt vmcnt(31)
	v_mfma_f32_32x32x16_f16 v[2:17], v[248:251], v[198:201], v[2:17]
	s_waitcnt vmcnt(30)
	v_mfma_f32_32x32x16_f16 v[18:33], v[252:255], v[198:201], v[18:33]
	s_waitcnt vmcnt(29)
	v_mfma_f32_32x32x16_f16 v[82:97], v[210:213], v[198:201], v[82:97]
	s_add_i32 s5, s7, 0xffffe400
	s_mov_b32 s22, s26
	s_mov_b32 s23, s27
	buffer_store_dwordx4 v[98:101], v1, s[20:23], s5 offen
	s_add_i32 s5, s7, 0xffffe800
	buffer_store_dwordx4 v[102:105], v1, s[20:23], s5 offen
	s_add_i32 s5, s7, 0xffffec00
	buffer_store_dwordx4 v[106:109], v1, s[20:23], s5 offen
	s_add_i32 s5, s7, 0xfffff000
	buffer_store_dwordx4 v[110:113], v1, s[20:23], s5 offen
	s_add_i32 s5, s7, 0xfffff400
	s_nop 0
	buffer_store_dwordx4 v[82:85], v1, s[20:23], s5 offen
	s_add_i32 s5, s7, 0xfffff800
	buffer_store_dwordx4 v[86:89], v1, s[20:23], s5 offen
	s_add_i32 s5, s7, 0xfffffc00
	buffer_store_dwordx4 v[90:93], v1, s[20:23], s5 offen
	buffer_store_dwordx4 v[94:97], v1, s[20:23], s7 offen
	s_add_i32 s6, s6, 0xa800
	s_add_i32 s4, s4, 1
	s_add_i32 s7, s7, 0xc000
	s_add_u32 s0, s0, 4
	s_addc_u32 s1, s1, 0
	s_mov_b32 s40, s41
	s_mov_b32 s41, s42
	s_mov_b32 s42, s43
	s_mov_b32 s43, s44
	s_mov_b32 s44, s45
	s_mov_b32 s45, s46
	s_mov_b32 s46, s47
	s_cmp_eq_u32 s6, 0x54000
	s_cbranch_scc0 .LBB2_2
	s_add_u32 s0, s10, s28
	s_addc_u32 s1, s11, 0
	s_waitcnt vmcnt(33)
	v_lshl_add_u64 v[50:51], s[0:1], 0, v[226:227]
	global_store_dword v[50:51], v34, off
	global_store_dword v[50:51], v35, off offset:768
	global_store_dword v[50:51], v36, off offset:1536
	global_store_dword v[50:51], v37, off offset:2304
	v_add_co_u32_e32 v34, vcc, 0x1000, v50
	s_mov_b64 s[4:5], 0
	s_nop 0
	v_addc_co_u32_e32 v35, vcc, 0, v51, vcc
	global_store_dword v[34:35], v38, off offset:2048
	global_store_dword v[34:35], v39, off offset:2816
	global_store_dword v[34:35], v40, off offset:3584
	v_add_co_u32_e32 v34, vcc, 0x2000, v50
	s_nop 1
	v_addc_co_u32_e32 v35, vcc, 0, v51, vcc
	global_store_dword v[34:35], v41, off offset:256
	v_add_co_u32_e32 v34, vcc, 0x3000, v50
	s_nop 1
	v_addc_co_u32_e32 v35, vcc, 0, v51, vcc
	global_store_dword v[34:35], v42, off
	global_store_dword v[34:35], v43, off offset:768
	global_store_dword v[34:35], v44, off offset:1536
	global_store_dword v[34:35], v45, off offset:2304
	v_add_co_u32_e32 v34, vcc, 0x4000, v50
	s_nop 1
	v_addc_co_u32_e32 v35, vcc, 0, v51, vcc
	global_store_dword v[34:35], v46, off offset:2048
	global_store_dword v[34:35], v47, off offset:2816
	global_store_dword v[34:35], v48, off offset:3584
	v_add_co_u32_e32 v34, vcc, 0x5000, v50
	s_nop 1
	v_addc_co_u32_e32 v35, vcc, 0, v51, vcc
	global_store_dword v[34:35], v49, off offset:256
	v_add_co_u32_e32 v34, vcc, 0x6000, v50
	s_nop 1
	v_addc_co_u32_e32 v35, vcc, 0, v51, vcc
	global_store_dword v[34:35], v2, off
	global_store_dword v[34:35], v3, off offset:768
	global_store_dword v[34:35], v4, off offset:1536
	global_store_dword v[34:35], v5, off offset:2304
	v_add_co_u32_e32 v2, vcc, 0x7000, v50
	s_nop 1
	v_addc_co_u32_e32 v3, vcc, 0, v51, vcc
	global_store_dword v[2:3], v6, off offset:2048
	global_store_dword v[2:3], v7, off offset:2816
	global_store_dword v[2:3], v8, off offset:3584
	v_add_co_u32_e32 v2, vcc, 0x8000, v50
	s_nop 1
	v_addc_co_u32_e32 v3, vcc, 0, v51, vcc
	global_store_dword v[2:3], v9, off offset:256
	v_add_co_u32_e32 v2, vcc, 0x9000, v50
	s_nop 1
	v_addc_co_u32_e32 v3, vcc, 0, v51, vcc
	global_store_dword v[2:3], v10, off
	global_store_dword v[2:3], v11, off offset:768
	global_store_dword v[2:3], v12, off offset:1536
	global_store_dword v[2:3], v13, off offset:2304
	v_add_co_u32_e32 v2, vcc, 0xa000, v50
	s_nop 1
	v_addc_co_u32_e32 v3, vcc, 0, v51, vcc
	global_store_dword v[2:3], v14, off offset:2048
	global_store_dword v[2:3], v15, off offset:2816
	global_store_dword v[2:3], v16, off offset:3584
	v_add_co_u32_e32 v2, vcc, 0xb000, v50
	s_nop 1
	v_addc_co_u32_e32 v3, vcc, 0, v51, vcc
	global_store_dword v[2:3], v17, off offset:256
	v_add_co_u32_e32 v2, vcc, 0xc000, v50
	s_nop 1
	v_addc_co_u32_e32 v3, vcc, 0, v51, vcc
	global_store_dword v[2:3], v18, off
	global_store_dword v[2:3], v19, off offset:768
	global_store_dword v[2:3], v20, off offset:1536
	global_store_dword v[2:3], v21, off offset:2304
	v_add_co_u32_e32 v2, vcc, 0xd000, v50
	s_nop 1
	v_addc_co_u32_e32 v3, vcc, 0, v51, vcc
	global_store_dword v[2:3], v22, off offset:2048
	global_store_dword v[2:3], v23, off offset:2816
	global_store_dword v[2:3], v24, off offset:3584
	v_add_co_u32_e32 v2, vcc, 0xe000, v50
	s_nop 1
	v_addc_co_u32_e32 v3, vcc, 0, v51, vcc
	global_store_dword v[2:3], v25, off offset:256
	v_add_co_u32_e32 v2, vcc, 0xf000, v50
	s_nop 1
	v_addc_co_u32_e32 v3, vcc, 0, v51, vcc
	global_store_dword v[2:3], v26, off
	global_store_dword v[2:3], v27, off offset:768
	global_store_dword v[2:3], v28, off offset:1536
	global_store_dword v[2:3], v29, off offset:2304
	v_add_co_u32_e32 v2, vcc, 0x10000, v50
	s_nop 1
	v_addc_co_u32_e32 v3, vcc, 0, v51, vcc
	global_store_dword v[2:3], v30, off offset:2048
	global_store_dword v[2:3], v31, off offset:2816
	global_store_dword v[2:3], v32, off offset:3584
	v_add_co_u32_e32 v2, vcc, 0x11000, v50
	s_nop 1
	v_addc_co_u32_e32 v3, vcc, 0, v51, vcc
	global_store_dword v[2:3], v33, off offset:256
